# speedup vs baseline: 1.0117x; 1.0084x over previous
.Lpp_w1:
	v_add_u32_e32 v6, 0x80, v6
	v_add_u32_e32 v7, 0xc80, v6
	v_add_u32_e32 v8, 0x1900, v6
	v_add_u32_e32 v9, 0x2580, v6
	v_subrev_u32_e32 v10, 18, v2
	v_mul_u32_u24_e32 v11, 0xc0, v3
	v_lshl_add_u32 v11, v10, 2, v11
	v_subrev_u32_e32 v12, 24, v11
	v_cmp_gt_u32_e32 vcc, 24, v2
	v_mov_b32_e32 v164, s8
	v_mov_b32_e32 v165, s9
	v_mov_b32_e32 v166, s6
	v_mov_b32_e32 v167, s7
	v_cndmask_b32_e32 v162, v164, v166, vcc
	v_cndmask_b32_e32 v163, v165, v167, vcc
	v_cndmask_b32_e32 v164, v12, v11, vcc
	s_nop 1
	v_add_co_u32_e32 v162, vcc, v162, v164
	s_nop 1
	v_addc_co_u32_e32 v163, vcc, 0, v163, vcc
	s_mov_b32 exec_lo, 0x3ffff
	s_mov_b32 exec_hi, 0x3ffff
	global_load_dword v48, v6, s[10:11] offset:0
	global_load_dword v49, v6, s[10:11] offset:200
	global_load_dword v50, v6, s[10:11] offset:400
	global_load_dword v51, v6, s[10:11] offset:600
	global_load_dword v52, v6, s[10:11] offset:800
	global_load_dword v53, v6, s[10:11] offset:1000
	global_load_dword v54, v6, s[10:11] offset:1200
	global_load_dword v55, v6, s[10:11] offset:1400
	global_load_dword v56, v7, s[10:11] offset:0
	global_load_dword v57, v7, s[10:11] offset:200
	global_load_dword v58, v7, s[10:11] offset:400
	global_load_dword v59, v7, s[10:11] offset:600
	global_load_dword v60, v7, s[10:11] offset:800
	global_load_dword v61, v7, s[10:11] offset:1000
	global_load_dword v62, v7, s[10:11] offset:1200
	global_load_dword v63, v7, s[10:11] offset:1400
	global_load_dword v64, v8, s[10:11] offset:0
	global_load_dword v65, v8, s[10:11] offset:200
	global_load_dword v66, v8, s[10:11] offset:400
	global_load_dword v67, v8, s[10:11] offset:600
	global_load_dword v68, v8, s[10:11] offset:800
	global_load_dword v69, v8, s[10:11] offset:1000
	global_load_dword v70, v8, s[10:11] offset:1200
	global_load_dword v71, v8, s[10:11] offset:1400
	s_mov_b64 s[44:45], exec
	s_mov_b32 exec_hi, 0
	global_load_dword v72, v9, s[10:11] offset:0
	global_load_dword v73, v9, s[10:11] offset:200
	s_mov_b64 exec, s[44:45]
	s_mov_b32 exec_lo, 0x3ffc0000
	s_mov_b32 exec_hi, 0x3ffc0000
	global_load_dword v48, v[162:163], off offset:0
	global_load_dword v49, v[162:163], off offset:24
	global_load_dword v50, v[162:163], off offset:48
	global_load_dword v51, v[162:163], off offset:72
	global_load_dword v52, v[162:163], off offset:96
	global_load_dword v53, v[162:163], off offset:120
	global_load_dword v54, v[162:163], off offset:144
	global_load_dword v55, v[162:163], off offset:168
	global_load_dword v56, v[162:163], off offset:384
	global_load_dword v57, v[162:163], off offset:408
	global_load_dword v58, v[162:163], off offset:432
	global_load_dword v59, v[162:163], off offset:456
	global_load_dword v60, v[162:163], off offset:480
	global_load_dword v61, v[162:163], off offset:504
	global_load_dword v62, v[162:163], off offset:528
	global_load_dword v63, v[162:163], off offset:552
	global_load_dword v64, v[162:163], off offset:768
	global_load_dword v65, v[162:163], off offset:792
	global_load_dword v66, v[162:163], off offset:816
	global_load_dword v67, v[162:163], off offset:840
	global_load_dword v68, v[162:163], off offset:864
	global_load_dword v69, v[162:163], off offset:888
	global_load_dword v70, v[162:163], off offset:912
	global_load_dword v71, v[162:163], off offset:936
	s_mov_b32 exec_hi, 0
	global_load_dword v72, v[162:163], off offset:1152
	global_load_dword v73, v[162:163], off offset:1176
	s_mov_b64 exec, -1
	s_waitcnt vmcnt(52)
	v_cvt_pk_f16_f32 v80, v16, v17
	v_cvt_pk_f16_f32 v81, v18, v19
	v_cvt_pk_f16_f32 v82, v20, v21
	v_cvt_pk_f16_f32 v83, v22, v23
	v_cvt_pk_f16_f32 v84, v24, v25
	v_cvt_pk_f16_f32 v85, v26, v27
	v_cvt_pk_f16_f32 v86, v28, v29
	v_cvt_pk_f16_f32 v87, v30, v31
	v_cvt_pk_f16_f32 v88, v32, v33
	v_cvt_pk_f16_f32 v89, v34, v35
	v_cvt_pk_f16_f32 v90, v36, v37
	v_cvt_pk_f16_f32 v91, v38, v39
	v_cvt_pk_f16_f32 v92, v40, v41
	v_cvt_pk_f16_f32 v93, v42, v43
	v_cvt_pk_f16_f32 v94, v44, v45
	v_cvt_pk_f16_f32 v95, v46, v47
	v_cvt_f32_f16_e32 v160, v80
	v_cvt_f32_f16_sdwa v161, v80 dst_sel:DWORD dst_unused:UNUSED_PAD src0_sel:WORD_1
	v_sub_f32_e32 v160, v16, v160
	v_sub_f32_e32 v161, v17, v161
	v_cvt_pk_f16_f32 v96, v160, v161
	v_cvt_f32_f16_e32 v160, v81
	v_cvt_f32_f16_sdwa v161, v81 dst_sel:DWORD dst_unused:UNUSED_PAD src0_sel:WORD_1
	v_sub_f32_e32 v160, v18, v160
	v_sub_f32_e32 v161, v19, v161
	v_cvt_pk_f16_f32 v97, v160, v161
	v_cvt_f32_f16_e32 v160, v82
	v_cvt_f32_f16_sdwa v161, v82 dst_sel:DWORD dst_unused:UNUSED_PAD src0_sel:WORD_1
	v_sub_f32_e32 v160, v20, v160
	v_sub_f32_e32 v161, v21, v161
	v_cvt_pk_f16_f32 v98, v160, v161
	v_cvt_f32_f16_e32 v160, v83
	v_cvt_f32_f16_sdwa v161, v83 dst_sel:DWORD dst_unused:UNUSED_PAD src0_sel:WORD_1
	v_sub_f32_e32 v160, v22, v160
	v_sub_f32_e32 v161, v23, v161
	v_cvt_pk_f16_f32 v99, v160, v161
	v_cvt_f32_f16_e32 v160, v84
	v_cvt_f32_f16_sdwa v161, v84 dst_sel:DWORD dst_unused:UNUSED_PAD src0_sel:WORD_1
	v_sub_f32_e32 v160, v24, v160
	v_sub_f32_e32 v161, v25, v161
	v_cvt_pk_f16_f32 v100, v160, v161
	v_cvt_f32_f16_e32 v160, v85
	v_cvt_f32_f16_sdwa v161, v85 dst_sel:DWORD dst_unused:UNUSED_PAD src0_sel:WORD_1
	v_sub_f32_e32 v160, v26, v160
	v_sub_f32_e32 v161, v27, v161
	v_cvt_pk_f16_f32 v101, v160, v161
	v_cvt_f32_f16_e32 v160, v86
	v_cvt_f32_f16_sdwa v161, v86 dst_sel:DWORD dst_unused:UNUSED_PAD src0_sel:WORD_1
	v_sub_f32_e32 v160, v28, v160
	v_sub_f32_e32 v161, v29, v161
	v_cvt_pk_f16_f32 v102, v160, v161
	v_cvt_f32_f16_e32 v160, v87
	v_cvt_f32_f16_sdwa v161, v87 dst_sel:DWORD dst_unused:UNUSED_PAD src0_sel:WORD_1
	v_sub_f32_e32 v160, v30, v160
	v_sub_f32_e32 v161, v31, v161
	v_cvt_pk_f16_f32 v103, v160, v161
	v_cvt_f32_f16_e32 v160, v88
	v_cvt_f32_f16_sdwa v161, v88 dst_sel:DWORD dst_unused:UNUSED_PAD src0_sel:WORD_1
	v_sub_f32_e32 v160, v32, v160
	v_sub_f32_e32 v161, v33, v161
	v_cvt_pk_f16_f32 v104, v160, v161
	v_cvt_f32_f16_e32 v160, v89
	v_cvt_f32_f16_sdwa v161, v89 dst_sel:DWORD dst_unused:UNUSED_PAD src0_sel:WORD_1
	v_sub_f32_e32 v160, v34, v160
	v_sub_f32_e32 v161, v35, v161
	v_cvt_pk_f16_f32 v105, v160, v161
	v_cvt_f32_f16_e32 v160, v90
	v_cvt_f32_f16_sdwa v161, v90 dst_sel:DWORD dst_unused:UNUSED_PAD src0_sel:WORD_1
	v_sub_f32_e32 v160, v36, v160
	v_sub_f32_e32 v161, v37, v161
	v_cvt_pk_f16_f32 v106, v160, v161
	v_cvt_f32_f16_e32 v160, v91
	v_cvt_f32_f16_sdwa v161, v91 dst_sel:DWORD dst_unused:UNUSED_PAD src0_sel:WORD_1
	v_sub_f32_e32 v160, v38, v160
	v_sub_f32_e32 v161, v39, v161
	v_cvt_pk_f16_f32 v107, v160, v161
	v_cvt_f32_f16_e32 v160, v92
	v_cvt_f32_f16_sdwa v161, v92 dst_sel:DWORD dst_unused:UNUSED_PAD src0_sel:WORD_1
	v_sub_f32_e32 v160, v40, v160
	v_sub_f32_e32 v161, v41, v161
	v_cvt_pk_f16_f32 v108, v160, v161
	v_cvt_f32_f16_e32 v160, v93
	v_cvt_f32_f16_sdwa v161, v93 dst_sel:DWORD dst_unused:UNUSED_PAD src0_sel:WORD_1
	v_sub_f32_e32 v160, v42, v160
	v_sub_f32_e32 v161, v43, v161
	v_cvt_pk_f16_f32 v109, v160, v161
	v_cvt_f32_f16_e32 v160, v94
	v_cvt_f32_f16_sdwa v161, v94 dst_sel:DWORD dst_unused:UNUSED_PAD src0_sel:WORD_1
	v_sub_f32_e32 v160, v44, v160
	v_sub_f32_e32 v161, v45, v161
	v_cvt_pk_f16_f32 v110, v160, v161
	v_cvt_f32_f16_e32 v160, v95
	v_cvt_f32_f16_sdwa v161, v95 dst_sel:DWORD dst_unused:UNUSED_PAD src0_sel:WORD_1
	v_sub_f32_e32 v160, v46, v160
	v_sub_f32_e32 v161, v47, v161
	v_cvt_pk_f16_f32 v111, v160, v161
	s_waitcnt vmcnt(0)
	v_cvt_pk_f16_f32 v112, v48, v49
	v_cvt_pk_f16_f32 v113, v50, v51
	v_cvt_pk_f16_f32 v114, v52, v53
	v_cvt_pk_f16_f32 v115, v54, v55
	v_cvt_pk_f16_f32 v116, v56, v57
	v_cvt_pk_f16_f32 v117, v58, v59
	v_cvt_pk_f16_f32 v118, v60, v61
	v_cvt_pk_f16_f32 v119, v62, v63
	v_cvt_pk_f16_f32 v120, v64, v65
	v_cvt_pk_f16_f32 v121, v66, v67
	v_cvt_pk_f16_f32 v122, v68, v69
	v_cvt_pk_f16_f32 v123, v70, v71
	v_cvt_pk_f16_f32 v124, v72, v73
	v_cvt_pk_f16_f32 v125, v74, v75
	v_cvt_pk_f16_f32 v126, v76, v77
	v_cvt_pk_f16_f32 v127, v78, v79
	v_cvt_f32_f16_e32 v160, v112
	v_cvt_f32_f16_sdwa v161, v112 dst_sel:DWORD dst_unused:UNUSED_PAD src0_sel:WORD_1
	v_sub_f32_e32 v160, v48, v160
	v_sub_f32_e32 v161, v49, v161
	v_cvt_pk_f16_f32 v128, v160, v161
	v_cvt_f32_f16_e32 v160, v113
	v_cvt_f32_f16_sdwa v161, v113 dst_sel:DWORD dst_unused:UNUSED_PAD src0_sel:WORD_1
	v_sub_f32_e32 v160, v50, v160
	v_sub_f32_e32 v161, v51, v161
	v_cvt_pk_f16_f32 v129, v160, v161
	v_cvt_f32_f16_e32 v160, v114
	v_cvt_f32_f16_sdwa v161, v114 dst_sel:DWORD dst_unused:UNUSED_PAD src0_sel:WORD_1
	v_sub_f32_e32 v160, v52, v160
	v_sub_f32_e32 v161, v53, v161
	v_cvt_pk_f16_f32 v130, v160, v161
	v_cvt_f32_f16_e32 v160, v115
	v_cvt_f32_f16_sdwa v161, v115 dst_sel:DWORD dst_unused:UNUSED_PAD src0_sel:WORD_1
	v_sub_f32_e32 v160, v54, v160
	v_sub_f32_e32 v161, v55, v161
	v_cvt_pk_f16_f32 v131, v160, v161
	v_cvt_f32_f16_e32 v160, v116
	v_cvt_f32_f16_sdwa v161, v116 dst_sel:DWORD dst_unused:UNUSED_PAD src0_sel:WORD_1
	v_sub_f32_e32 v160, v56, v160
	v_sub_f32_e32 v161, v57, v161
	v_cvt_pk_f16_f32 v132, v160, v161
	v_cvt_f32_f16_e32 v160, v117
	v_cvt_f32_f16_sdwa v161, v117 dst_sel:DWORD dst_unused:UNUSED_PAD src0_sel:WORD_1
	v_sub_f32_e32 v160, v58, v160
	v_sub_f32_e32 v161, v59, v161
	v_cvt_pk_f16_f32 v133, v160, v161
	v_cvt_f32_f16_e32 v160, v118
	v_cvt_f32_f16_sdwa v161, v118 dst_sel:DWORD dst_unused:UNUSED_PAD src0_sel:WORD_1
	v_sub_f32_e32 v160, v60, v160
	v_sub_f32_e32 v161, v61, v161
	v_cvt_pk_f16_f32 v134, v160, v161
	v_cvt_f32_f16_e32 v160, v119
	v_cvt_f32_f16_sdwa v161, v119 dst_sel:DWORD dst_unused:UNUSED_PAD src0_sel:WORD_1
	v_sub_f32_e32 v160, v62, v160
	v_sub_f32_e32 v161, v63, v161
	v_cvt_pk_f16_f32 v135, v160, v161
	v_cvt_f32_f16_e32 v160, v120
	v_cvt_f32_f16_sdwa v161, v120 dst_sel:DWORD dst_unused:UNUSED_PAD src0_sel:WORD_1
	v_sub_f32_e32 v160, v64, v160
	v_sub_f32_e32 v161, v65, v161
	v_cvt_pk_f16_f32 v136, v160, v161
	v_cvt_f32_f16_e32 v160, v121
	v_cvt_f32_f16_sdwa v161, v121 dst_sel:DWORD dst_unused:UNUSED_PAD src0_sel:WORD_1
	v_sub_f32_e32 v160, v66, v160
	v_sub_f32_e32 v161, v67, v161
	v_cvt_pk_f16_f32 v137, v160, v161
	v_cvt_f32_f16_e32 v160, v122
	v_cvt_f32_f16_sdwa v161, v122 dst_sel:DWORD dst_unused:UNUSED_PAD src0_sel:WORD_1
	v_sub_f32_e32 v160, v68, v160
	v_sub_f32_e32 v161, v69, v161
	v_cvt_pk_f16_f32 v138, v160, v161
	v_cvt_f32_f16_e32 v160, v123
	v_cvt_f32_f16_sdwa v161, v123 dst_sel:DWORD dst_unused:UNUSED_PAD src0_sel:WORD_1
	v_sub_f32_e32 v160, v70, v160
	v_sub_f32_e32 v161, v71, v161
	v_cvt_pk_f16_f32 v139, v160, v161
	v_cvt_f32_f16_e32 v160, v124
	v_cvt_f32_f16_sdwa v161, v124 dst_sel:DWORD dst_unused:UNUSED_PAD src0_sel:WORD_1
	v_sub_f32_e32 v160, v72, v160
	v_sub_f32_e32 v161, v73, v161
	v_cvt_pk_f16_f32 v140, v160, v161
	v_cvt_f32_f16_e32 v160, v125
	v_cvt_f32_f16_sdwa v161, v125 dst_sel:DWORD dst_unused:UNUSED_PAD src0_sel:WORD_1
	v_sub_f32_e32 v160, v74, v160
	v_sub_f32_e32 v161, v75, v161
	v_cvt_pk_f16_f32 v141, v160, v161
	v_cvt_f32_f16_e32 v160, v126
	v_cvt_f32_f16_sdwa v161, v126 dst_sel:DWORD dst_unused:UNUSED_PAD src0_sel:WORD_1
	v_sub_f32_e32 v160, v76, v160
	v_sub_f32_e32 v161, v77, v161
	v_cvt_pk_f16_f32 v142, v160, v161
	v_cvt_f32_f16_e32 v160, v127
	v_cvt_f32_f16_sdwa v161, v127 dst_sel:DWORD dst_unused:UNUSED_PAD src0_sel:WORD_1
	v_sub_f32_e32 v160, v78, v160
	v_sub_f32_e32 v161, v79, v161
	v_cvt_pk_f16_f32 v143, v160, v161
	s_nop 1
	v_mfma_f32_32x32x16_f16 v[144:159], v[80:83], v[112:115], 0
	v_mfma_f32_32x32x16_f16 v[144:159], v[96:99], v[112:115], v[144:159]
	v_mfma_f32_32x32x16_f16 v[144:159], v[80:83], v[128:131], v[144:159]
	v_mfma_f32_32x32x16_f16 v[144:159], v[84:87], v[116:119], v[144:159]
	v_mfma_f32_32x32x16_f16 v[144:159], v[100:103], v[116:119], v[144:159]
	v_mfma_f32_32x32x16_f16 v[144:159], v[84:87], v[132:135], v[144:159]
	v_mfma_f32_32x32x16_f16 v[144:159], v[88:91], v[120:123], v[144:159]
	v_mfma_f32_32x32x16_f16 v[144:159], v[104:107], v[120:123], v[144:159]
	v_mfma_f32_32x32x16_f16 v[144:159], v[88:91], v[136:139], v[144:159]
	v_mfma_f32_32x32x16_f16 v[144:159], v[92:95], v[124:127], v[144:159]
	v_mfma_f32_32x32x16_f16 v[144:159], v[108:111], v[124:127], v[144:159]
	v_mfma_f32_32x32x16_f16 v[144:159], v[92:95], v[140:143], v[144:159]
	s_nop 15
	v_mul_u32_u24_e32 v13, 0xc0, v3
	v_lshl_add_u32 v13, v10, 2, v13
	s_mov_b32 exec_lo, 0x3ffc0000
	s_mov_b32 exec_hi, 0x3ffc0000
	ds_write_b32 v13, v144 offset:0
	ds_write_b32 v13, v145 offset:48
	ds_write_b32 v13, v146 offset:96
	ds_write_b32 v13, v147 offset:144
	ds_write_b32 v13, v148 offset:384
	ds_write_b32 v13, v149 offset:432
	ds_write_b32 v13, v150 offset:480
	ds_write_b32 v13, v151 offset:528
	ds_write_b32 v13, v152 offset:768
	ds_write_b32 v13, v153 offset:816
	ds_write_b32 v13, v154 offset:864
	ds_write_b32 v13, v155 offset:912
	ds_write_b32 v13, v156 offset:1152
	ds_write_b32 v13, v157 offset:1200
	ds_write_b32 v13, v158 offset:1248
	ds_write_b32 v13, v159 offset:1296
	s_mov_b64 exec, -1
	v_and_b32_e32 v160, 27, v2
	v_cmp_eq_u32_e32 vcc, 18, v160
	s_nop 1
	v_cndmask_b32_e64 v161, 0, 1.0, vcc
	v_cmp_lt_u32_e32 vcc, 17, v2
	s_nop 1
	v_cndmask_b32_e32 v144, v144, v161, vcc
	v_cndmask_b32_e32 v145, v145, v161, vcc
	v_cndmask_b32_e32 v146, v146, v161, vcc
	v_cndmask_b32_e32 v147, v147, v161, vcc
	v_cndmask_b32_e32 v148, v148, v161, vcc
	v_cndmask_b32_e32 v149, v149, v161, vcc
	v_cndmask_b32_e32 v150, v150, v161, vcc
	v_cndmask_b32_e32 v151, v151, v161, vcc
	v_cndmask_b32_e32 v152, v152, v161, vcc
	v_cndmask_b32_e32 v153, v153, v161, vcc
	v_cndmask_b32_e32 v154, v154, v161, vcc
	v_cndmask_b32_e32 v155, v155, v161, vcc
	v_cndmask_b32_e32 v156, v156, v161, vcc
	v_cndmask_b32_e32 v157, v157, v161, vcc
	v_cndmask_b32_e32 v158, v158, v161, vcc
	v_cndmask_b32_e32 v159, v159, v161, vcc
	s_movk_i32 s32, 0x800
